# baseline (speedup 1.0000x reference)
.LBB1_30:
	s_and_b64 vcc, exec, s[4:5]
	s_cbranch_vccz .LBB1_41
	s_sleep 45
	s_load_dwordx4 s[44:47], s[0:1], 0x0
	s_load_dwordx2 s[48:49], s[0:1], 0x20
	s_mov_b32 s50, s2
	v_and_b32_e32 v1, 31, v0
	v_lshrrev_b32_e32 v2, 5, v0
	v_lshlrev_b32_e32 v3, 5, v1
	v_lshl_add_u32 v3, v2, 13, v3
	v_add_u32_e32 v3, 0x1400, v3
	v_lshlrev_b32_e32 v4, 4, v1
	v_lshl_add_u32 v4, v2, 12, v4
	v_add_u32_e32 v4, 0xa00, v4
	s_waitcnt lgkmcnt(0)
	s_add_u32 s48, s48, 0x408000
	s_addc_u32 s49, s49, 0
	s_load_dwordx4 s[52:55], s[48:49], 0x800
	s_lshl_b32 s51, s50, 18
	s_add_u32 s44, s44, s51
	s_addc_u32 s45, s45, 0
	s_mul_i32 s51, s50, 0x30000
	s_add_u32 s46, s46, s51
	s_addc_u32 s47, s47, 0
	s_waitcnt lgkmcnt(0)
	s_lshl_b32 s51, s50, 19
	s_add_u32 s52, s52, s51
	s_addc_u32 s53, s53, 0
	s_mul_i32 s51, s50, 0x60000
	s_add_u32 s54, s54, s51
	s_addc_u32 s55, s55, 0
	v_cmp_eq_u32_e64 s[78:79], 0, v0
	v_mov_b32_e32 v5, 1
	v_mov_b32_e32 v6, s50
	v_lshlrev_b32_e32 v6, 2, v6
	s_add_u32 s58, s52, 0x0
	s_addc_u32 s59, s53, 0
	global_load_dwordx4 v[16:19], v3, s[58:59] nt
	global_load_dwordx4 v[20:23], v3, s[58:59] offset:16 nt
	s_add_u32 s58, s52, 0x20000
	s_addc_u32 s59, s53, 0
	global_load_dwordx4 v[24:27], v3, s[58:59] nt
	global_load_dwordx4 v[28:31], v3, s[58:59] offset:16 nt
	s_add_u32 s58, s52, 0x40000
	s_addc_u32 s59, s53, 0
	global_load_dwordx4 v[32:35], v3, s[58:59] nt
	global_load_dwordx4 v[36:39], v3, s[58:59] offset:16 nt
	s_add_u32 s58, s52, 0x60000
	s_addc_u32 s59, s53, 0
	global_load_dwordx4 v[40:43], v3, s[58:59] nt
	global_load_dwordx4 v[44:47], v3, s[58:59] offset:16 nt
	s_add_u32 s58, s54, 0x0
	s_addc_u32 s59, s55, 0
	global_load_dwordx4 v[48:51], v3, s[58:59] nt
	global_load_dwordx4 v[52:55], v3, s[58:59] offset:16 nt
	s_add_u32 s58, s54, 0x20000
	s_addc_u32 s59, s55, 0
	global_load_dwordx4 v[56:59], v3, s[58:59] nt
	global_load_dwordx4 v[60:63], v3, s[58:59] offset:16 nt
	s_add_u32 s58, s54, 0x40000
	s_addc_u32 s59, s55, 0
	global_load_dwordx4 v[64:67], v3, s[58:59] nt
	global_load_dwordx4 v[68:71], v3, s[58:59] offset:16 nt
	s_add_u32 s58, s52, 0x400
	s_addc_u32 s59, s53, 0
	global_load_dwordx4 v[72:75], v3, s[58:59] nt
	global_load_dwordx4 v[76:79], v3, s[58:59] offset:16 nt
	s_add_u32 s58, s52, 0x20400
	s_addc_u32 s59, s53, 0
	global_load_dwordx4 v[80:83], v3, s[58:59] nt
	global_load_dwordx4 v[84:87], v3, s[58:59] offset:16 nt
	s_add_u32 s58, s52, 0x40400
	s_addc_u32 s59, s53, 0
	global_load_dwordx4 v[88:91], v3, s[58:59] nt
	global_load_dwordx4 v[92:95], v3, s[58:59] offset:16 nt
	s_add_u32 s58, s52, 0x60400
	s_addc_u32 s59, s53, 0
	global_load_dwordx4 v[96:99], v3, s[58:59] nt
	global_load_dwordx4 v[100:103], v3, s[58:59] offset:16 nt
	s_add_u32 s58, s54, 0x400
	s_addc_u32 s59, s55, 0
	global_load_dwordx4 v[104:107], v3, s[58:59] nt
	global_load_dwordx4 v[108:111], v3, s[58:59] offset:16 nt
	s_add_u32 s58, s54, 0x20400
	s_addc_u32 s59, s55, 0
	global_load_dwordx4 v[112:115], v3, s[58:59] nt
	global_load_dwordx4 v[116:119], v3, s[58:59] offset:16 nt
	s_add_u32 s58, s54, 0x40400
	s_addc_u32 s59, s55, 0
	global_load_dwordx4 v[120:123], v3, s[58:59] nt
	global_load_dwordx4 v[124:127], v3, s[58:59] offset:16 nt
	s_waitcnt vmcnt(26)
	v_cvt_pk_f16_f32 v16, v16, v17
	v_cvt_pk_f16_f32 v17, v18, v19
	v_cvt_pk_f16_f32 v18, v20, v21
	v_cvt_pk_f16_f32 v19, v22, v23
	s_add_u32 s76, s44, 0x0
	s_addc_u32 s77, s45, 0
	global_store_dwordx4 v4, v[16:19], s[76:77] sc1
	s_waitcnt vmcnt(25)
	v_cvt_pk_f16_f32 v24, v24, v25
	v_cvt_pk_f16_f32 v25, v26, v27
	v_cvt_pk_f16_f32 v26, v28, v29
	v_cvt_pk_f16_f32 v27, v30, v31
	s_add_u32 s76, s44, 0x10000
	s_addc_u32 s77, s45, 0
	global_store_dwordx4 v4, v[24:27], s[76:77] sc1
	s_waitcnt vmcnt(24)
	v_cvt_pk_f16_f32 v32, v32, v33
	v_cvt_pk_f16_f32 v33, v34, v35
	v_cvt_pk_f16_f32 v34, v36, v37
	v_cvt_pk_f16_f32 v35, v38, v39
	s_add_u32 s76, s44, 0x20000
	s_addc_u32 s77, s45, 0
	global_store_dwordx4 v4, v[32:35], s[76:77] sc1
	s_waitcnt vmcnt(23)
	v_cvt_pk_f16_f32 v40, v40, v41
	v_cvt_pk_f16_f32 v41, v42, v43
	v_cvt_pk_f16_f32 v42, v44, v45
	v_cvt_pk_f16_f32 v43, v46, v47
	s_add_u32 s76, s44, 0x30000
	s_addc_u32 s77, s45, 0
	global_store_dwordx4 v4, v[40:43], s[76:77] sc1
	s_waitcnt vmcnt(22)
	v_cvt_pk_f16_f32 v48, v48, v49
	v_cvt_pk_f16_f32 v49, v50, v51
	v_cvt_pk_f16_f32 v50, v52, v53
	v_cvt_pk_f16_f32 v51, v54, v55
	s_add_u32 s76, s46, 0x0
	s_addc_u32 s77, s47, 0
	global_store_dwordx4 v4, v[48:51], s[76:77] sc1
	s_waitcnt vmcnt(21)
	v_cvt_pk_f16_f32 v56, v56, v57
	v_cvt_pk_f16_f32 v57, v58, v59
	v_cvt_pk_f16_f32 v58, v60, v61
	v_cvt_pk_f16_f32 v59, v62, v63
	s_add_u32 s76, s46, 0x10000
	s_addc_u32 s77, s47, 0
	global_store_dwordx4 v4, v[56:59], s[76:77] sc1
	s_waitcnt vmcnt(20)
	v_cvt_pk_f16_f32 v64, v64, v65
	v_cvt_pk_f16_f32 v65, v66, v67
	v_cvt_pk_f16_f32 v66, v68, v69
	v_cvt_pk_f16_f32 v67, v70, v71
	s_add_u32 s76, s46, 0x20000
	s_addc_u32 s77, s47, 0
	global_store_dwordx4 v4, v[64:67], s[76:77] sc1
	s_add_u32 s58, s52, 0x800
	s_addc_u32 s59, s53, 0
	global_load_dwordx4 v[16:19], v3, s[58:59] nt
	global_load_dwordx4 v[20:23], v3, s[58:59] offset:16 nt
	s_add_u32 s58, s52, 0x20800
	s_addc_u32 s59, s53, 0
	global_load_dwordx4 v[24:27], v3, s[58:59] nt
	global_load_dwordx4 v[28:31], v3, s[58:59] offset:16 nt
	s_add_u32 s58, s52, 0x40800
	s_addc_u32 s59, s53, 0
	global_load_dwordx4 v[32:35], v3, s[58:59] nt
	global_load_dwordx4 v[36:39], v3, s[58:59] offset:16 nt
	s_add_u32 s58, s52, 0x60800
	s_addc_u32 s59, s53, 0
	global_load_dwordx4 v[40:43], v3, s[58:59] nt
	global_load_dwordx4 v[44:47], v3, s[58:59] offset:16 nt
	s_add_u32 s58, s54, 0x800
	s_addc_u32 s59, s55, 0
	global_load_dwordx4 v[48:51], v3, s[58:59] nt
	global_load_dwordx4 v[52:55], v3, s[58:59] offset:16 nt
	s_add_u32 s58, s54, 0x20800
	s_addc_u32 s59, s55, 0
	global_load_dwordx4 v[56:59], v3, s[58:59] nt
	global_load_dwordx4 v[60:63], v3, s[58:59] offset:16 nt
	s_add_u32 s58, s54, 0x40800
	s_addc_u32 s59, s55, 0
	global_load_dwordx4 v[64:67], v3, s[58:59] nt
	global_load_dwordx4 v[68:71], v3, s[58:59] offset:16 nt
	s_waitcnt vmcnt(33)
	v_cvt_pk_f16_f32 v72, v72, v73
	v_cvt_pk_f16_f32 v73, v74, v75
	v_cvt_pk_f16_f32 v74, v76, v77
	v_cvt_pk_f16_f32 v75, v78, v79
	s_add_u32 s76, s44, 0x200
	s_addc_u32 s77, s45, 0
	global_store_dwordx4 v4, v[72:75], s[76:77] sc1
	s_waitcnt vmcnt(32)
	v_cvt_pk_f16_f32 v80, v80, v81
	v_cvt_pk_f16_f32 v81, v82, v83
	v_cvt_pk_f16_f32 v82, v84, v85
	v_cvt_pk_f16_f32 v83, v86, v87
	s_add_u32 s76, s44, 0x10200
	s_addc_u32 s77, s45, 0
	global_store_dwordx4 v4, v[80:83], s[76:77] sc1
	s_waitcnt vmcnt(31)
	v_cvt_pk_f16_f32 v88, v88, v89
	v_cvt_pk_f16_f32 v89, v90, v91
	v_cvt_pk_f16_f32 v90, v92, v93
	v_cvt_pk_f16_f32 v91, v94, v95
	s_add_u32 s76, s44, 0x20200
	s_addc_u32 s77, s45, 0
	global_store_dwordx4 v4, v[88:91], s[76:77] sc1
	s_waitcnt vmcnt(30)
	v_cvt_pk_f16_f32 v96, v96, v97
	v_cvt_pk_f16_f32 v97, v98, v99
	v_cvt_pk_f16_f32 v98, v100, v101
	v_cvt_pk_f16_f32 v99, v102, v103
	s_add_u32 s76, s44, 0x30200
	s_addc_u32 s77, s45, 0
	global_store_dwordx4 v4, v[96:99], s[76:77] sc1
	s_waitcnt vmcnt(29)
	v_cvt_pk_f16_f32 v104, v104, v105
	v_cvt_pk_f16_f32 v105, v106, v107
	v_cvt_pk_f16_f32 v106, v108, v109
	v_cvt_pk_f16_f32 v107, v110, v111
	s_add_u32 s76, s46, 0x200
	s_addc_u32 s77, s47, 0
	global_store_dwordx4 v4, v[104:107], s[76:77] sc1
	s_waitcnt vmcnt(28)
	v_cvt_pk_f16_f32 v112, v112, v113
	v_cvt_pk_f16_f32 v113, v114, v115
	v_cvt_pk_f16_f32 v114, v116, v117
	v_cvt_pk_f16_f32 v115, v118, v119
	s_add_u32 s76, s46, 0x10200
	s_addc_u32 s77, s47, 0
	global_store_dwordx4 v4, v[112:115], s[76:77] sc1
	s_waitcnt vmcnt(27)
	v_cvt_pk_f16_f32 v120, v120, v121
	v_cvt_pk_f16_f32 v121, v122, v123
	v_cvt_pk_f16_f32 v122, v124, v125
	v_cvt_pk_f16_f32 v123, v126, v127
	s_add_u32 s76, s46, 0x20200
	s_addc_u32 s77, s47, 0
	global_store_dwordx4 v4, v[120:123], s[76:77] sc1
	s_waitcnt vmcnt(21)
	s_barrier
	s_mov_b64 s[56:57], exec
	s_and_b64 exec, exec, s[78:79]
	global_store_dword v6, v5, s[48:49] offset:0 sc1
	s_mov_b64 exec, s[56:57]
	s_waitcnt vmcnt(20)
	v_cvt_pk_f16_f32 v16, v16, v17
	v_cvt_pk_f16_f32 v17, v18, v19
	v_cvt_pk_f16_f32 v18, v20, v21
	v_cvt_pk_f16_f32 v19, v22, v23
	s_add_u32 s76, s44, 0x400
	s_addc_u32 s77, s45, 0
	global_store_dwordx4 v4, v[16:19], s[76:77] sc1
	s_waitcnt vmcnt(19)
	v_cvt_pk_f16_f32 v24, v24, v25
	v_cvt_pk_f16_f32 v25, v26, v27
	v_cvt_pk_f16_f32 v26, v28, v29
	v_cvt_pk_f16_f32 v27, v30, v31
	s_add_u32 s76, s44, 0x10400
	s_addc_u32 s77, s45, 0
	global_store_dwordx4 v4, v[24:27], s[76:77] sc1
	s_waitcnt vmcnt(18)
	v_cvt_pk_f16_f32 v32, v32, v33
	v_cvt_pk_f16_f32 v33, v34, v35
	v_cvt_pk_f16_f32 v34, v36, v37
	v_cvt_pk_f16_f32 v35, v38, v39
	s_add_u32 s76, s44, 0x20400
	s_addc_u32 s77, s45, 0
	global_store_dwordx4 v4, v[32:35], s[76:77] sc1
	s_waitcnt vmcnt(17)
	v_cvt_pk_f16_f32 v40, v40, v41
	v_cvt_pk_f16_f32 v41, v42, v43
	v_cvt_pk_f16_f32 v42, v44, v45
	v_cvt_pk_f16_f32 v43, v46, v47
	s_add_u32 s76, s44, 0x30400
	s_addc_u32 s77, s45, 0
	global_store_dwordx4 v4, v[40:43], s[76:77] sc1
	s_waitcnt vmcnt(16)
	v_cvt_pk_f16_f32 v48, v48, v49
	v_cvt_pk_f16_f32 v49, v50, v51
	v_cvt_pk_f16_f32 v50, v52, v53
	v_cvt_pk_f16_f32 v51, v54, v55
	s_add_u32 s76, s46, 0x400
	s_addc_u32 s77, s47, 0
	global_store_dwordx4 v4, v[48:51], s[76:77] sc1
	s_waitcnt vmcnt(15)
	v_cvt_pk_f16_f32 v56, v56, v57
	v_cvt_pk_f16_f32 v57, v58, v59
	v_cvt_pk_f16_f32 v58, v60, v61
	v_cvt_pk_f16_f32 v59, v62, v63
	s_add_u32 s76, s46, 0x10400
	s_addc_u32 s77, s47, 0
	global_store_dwordx4 v4, v[56:59], s[76:77] sc1
	s_waitcnt vmcnt(14)
	v_cvt_pk_f16_f32 v64, v64, v65
	v_cvt_pk_f16_f32 v65, v66, v67
	v_cvt_pk_f16_f32 v66, v68, v69
	v_cvt_pk_f16_f32 v67, v70, v71
	s_add_u32 s76, s46, 0x20400
	s_addc_u32 s77, s47, 0
	global_store_dwordx4 v4, v[64:67], s[76:77] sc1
	s_waitcnt vmcnt(8)
	s_barrier
	s_mov_b64 s[56:57], exec
	s_and_b64 exec, exec, s[78:79]
	global_store_dword v6, v5, s[48:49] offset:256 sc1
	s_mov_b64 exec, s[56:57]
	s_waitcnt vmcnt(1)
	s_barrier
	s_mov_b64 s[56:57], exec
	s_and_b64 exec, exec, s[78:79]
	global_store_dword v6, v5, s[48:49] offset:512 sc1
	s_mov_b64 exec, s[56:57]
	s_mov_b32 s24, s2
	s_lshl_b32 s20, s24, 4
	s_lshl_b32 s0, s24, 5
	s_ashr_i32 s21, s20, 31
	s_and_b32 s25, s0, 0xffffffc0
	s_lshl_b64 s[20:21], s[20:21], 2
	v_lshrrev_b32_e32 v6, 6, v0
	s_waitcnt lgkmcnt(0)
	s_add_u32 s26, s30, s20
	s_addc_u32 s27, s31, s21
	v_lshl_or_b32 v2, v6, 3, s25
	s_and_b32 s25, s2, 1
	s_lshl_b32 s2, s25, 7
	s_add_u32 s20, s28, s2
	v_and_b32_e32 v7, 63, v0
	s_mov_b32 s3, 0
	s_addc_u32 s21, s29, 0
	s_bfe_u32 s2, s24, 0x1a0001
	v_add_u32_e32 v2, v2, v7
	v_mov_b32_e32 v3, 0
	s_lshl_b64 s[2:3], s[2:3], 19
	v_lshl_add_u32 v1, v6, 2, 0
	v_lshlrev_b64 v[4:5], 8, v[2:3]
	v_lshl_or_b32 v2, v6, 16, s2
	s_lshl_b32 s2, s25, 12
	v_lshlrev_b32_e32 v6, 2, v7
	v_cmp_gt_u32_e64 s[0:1], 8, v7
	v_cmp_eq_u32_e64 s[22:23], 0, v7
	v_cmp_eq_u32_e64 s[6:7], 1, v7
	v_cmp_eq_u32_e64 s[8:9], 2, v7
	v_cmp_eq_u32_e64 s[10:11], 3, v7
	v_cmp_eq_u32_e64 s[12:13], 4, v7
	v_cmp_eq_u32_e64 s[14:15], 5, v7
	v_cmp_eq_u32_e64 s[16:17], 6, v7
	v_cmp_eq_u32_e64 s[18:19], 7, v7
	v_or3_b32 v6, v2, s2, v6
	v_mov_b32_e32 v7, s3
	v_cmp_eq_u32_e64 s[4:5], 0, v0
	v_lshl_add_u64 v[4:5], s[20:21], 0, v[4:5]
	v_lshl_add_u64 v[6:7], s[42:43], 0, v[6:7]
	s_mov_b64 s[28:29], 0
	s_lshr_b32 s58, s24, 1
	s_lshl_b32 s58, s58, 19
	s_add_u32 s60, s42, s58
	s_addc_u32 s61, s43, 0
	s_add_u32 s62, s60, 0x2000
	s_addc_u32 s63, s61, 0
	s_add_u32 s64, s62, 0x2000
	s_addc_u32 s65, s63, 0
	s_add_u32 s66, s64, 0x2000
	s_addc_u32 s67, s65, 0
	s_add_u32 s68, s66, 0x2000
	s_addc_u32 s69, s67, 0
	s_add_u32 s70, s68, 0x2000
	s_addc_u32 s71, s69, 0
	s_add_u32 s72, s70, 0x2000
	s_addc_u32 s73, s71, 0
	s_add_u32 s74, s72, 0x2000
	s_addc_u32 s75, s73, 0
	v_lshrrev_b32_e32 v96, 6, v0
	v_lshlrev_b32_e32 v96, 16, v96
	v_and_b32_e32 v97, 63, v0
	v_lshl_add_u32 v96, v97, 2, v96
	s_and_b32 s59, s24, 1
	s_lshl_b32 s59, s59, 12
	v_add_u32_e32 v96, s59, v96
	s_mov_b32 s76, 0
	s_mov_b32 s77, 0
	global_load_dword v100, v96, s[60:61] offset:0 nt
	global_load_dword v101, v96, s[62:63] offset:0 nt
	global_load_dword v102, v96, s[64:65] offset:0 nt
	global_load_dword v103, v96, s[66:67] offset:0 nt
	global_load_dword v104, v96, s[68:69] offset:0 nt
	global_load_dword v105, v96, s[70:71] offset:0 nt
	global_load_dword v106, v96, s[72:73] offset:0 nt
	global_load_dword v107, v96, s[74:75] offset:0 nt
	global_load_dword v108, v96, s[60:61] offset:256 nt
	global_load_dword v109, v96, s[62:63] offset:256 nt
	global_load_dword v110, v96, s[64:65] offset:256 nt
	global_load_dword v111, v96, s[66:67] offset:256 nt
	global_load_dword v112, v96, s[68:69] offset:256 nt
	global_load_dword v113, v96, s[70:71] offset:256 nt
	global_load_dword v114, v96, s[72:73] offset:256 nt
	global_load_dword v115, v96, s[74:75] offset:256 nt
	global_load_dword v116, v96, s[60:61] offset:512 nt
	global_load_dword v117, v96, s[62:63] offset:512 nt
	global_load_dword v118, v96, s[64:65] offset:512 nt
	global_load_dword v119, v96, s[66:67] offset:512 nt
	global_load_dword v120, v96, s[68:69] offset:512 nt
	global_load_dword v121, v96, s[70:71] offset:512 nt
	global_load_dword v122, v96, s[72:73] offset:512 nt
	global_load_dword v123, v96, s[74:75] offset:512 nt
	global_load_dword v124, v96, s[60:61] offset:768 nt
	global_load_dword v125, v96, s[62:63] offset:768 nt
	global_load_dword v126, v96, s[64:65] offset:768 nt
	global_load_dword v127, v96, s[66:67] offset:768 nt
	global_load_dword v128, v96, s[68:69] offset:768 nt
	global_load_dword v129, v96, s[70:71] offset:768 nt
	global_load_dword v130, v96, s[72:73] offset:768 nt
	global_load_dword v131, v96, s[74:75] offset:768 nt
	global_load_dword v132, v96, s[60:61] offset:1024 nt
	global_load_dword v133, v96, s[62:63] offset:1024 nt
	global_load_dword v134, v96, s[64:65] offset:1024 nt
	global_load_dword v135, v96, s[66:67] offset:1024 nt
	global_load_dword v136, v96, s[68:69] offset:1024 nt
	global_load_dword v137, v96, s[70:71] offset:1024 nt
	global_load_dword v138, v96, s[72:73] offset:1024 nt
	global_load_dword v139, v96, s[74:75] offset:1024 nt
	global_load_dword v140, v96, s[60:61] offset:1280 nt
	global_load_dword v141, v96, s[62:63] offset:1280 nt
	global_load_dword v142, v96, s[64:65] offset:1280 nt
	global_load_dword v143, v96, s[66:67] offset:1280 nt
	global_load_dword v144, v96, s[68:69] offset:1280 nt
	global_load_dword v145, v96, s[70:71] offset:1280 nt
	global_load_dword v146, v96, s[72:73] offset:1280 nt
	global_load_dword v147, v96, s[74:75] offset:1280 nt
	global_load_dword v148, v96, s[60:61] offset:1536 nt
	global_load_dword v149, v96, s[62:63] offset:1536 nt
	global_load_dword v150, v96, s[64:65] offset:1536 nt
	global_load_dword v151, v96, s[66:67] offset:1536 nt
	global_load_dword v152, v96, s[68:69] offset:1536 nt
	global_load_dword v153, v96, s[70:71] offset:1536 nt
	global_load_dword v154, v96, s[72:73] offset:1536 nt
	global_load_dword v155, v96, s[74:75] offset:1536 nt
	s_waitcnt vmcnt(48)
	v_cmp_ne_u32_e32 vcc, 0, v100
	s_nop 1
	v_mov_b32_e32 v2, vcc_lo
	v_mov_b32_e32 v9, vcc_hi
	v_cmp_ne_u32_e32 vcc, 0, v101
	v_cndmask_b32_e64 v2, 0, v2, s[22:23]
	v_cndmask_b32_e64 v9, 0, v9, s[22:23]
	v_mov_b32_e32 v11, vcc_hi
	v_mov_b32_e32 v14, vcc_lo
	v_cndmask_b32_e64 v9, v9, v11, s[6:7]
	v_cndmask_b32_e64 v2, v2, v14, s[6:7]
	v_cmp_ne_u32_e32 vcc, 0, v102
	s_nop 1
	v_mov_b32_e32 v11, vcc_lo
	v_mov_b32_e32 v14, vcc_hi
	v_cmp_ne_u32_e32 vcc, 0, v103
	v_cndmask_b32_e64 v2, v2, v11, s[8:9]
	v_cndmask_b32_e64 v9, v9, v14, s[8:9]
	v_mov_b32_e32 v11, vcc_hi
	v_mov_b32_e32 v14, vcc_lo
	v_cmp_ne_u32_e32 vcc, 0, v104
	v_cndmask_b32_e64 v9, v9, v11, s[10:11]
	v_cndmask_b32_e64 v2, v2, v14, s[10:11]
	v_mov_b32_e32 v11, vcc_lo
	v_mov_b32_e32 v12, vcc_hi
	v_cmp_ne_u32_e32 vcc, 0, v105
	v_cndmask_b32_e64 v2, v2, v11, s[12:13]
	v_cndmask_b32_e64 v9, v9, v12, s[12:13]
	v_mov_b32_e32 v11, vcc_hi
	v_mov_b32_e32 v12, vcc_lo
	v_cndmask_b32_e64 v9, v9, v11, s[14:15]
	v_cndmask_b32_e64 v2, v2, v12, s[14:15]
	v_cmp_ne_u32_e32 vcc, 0, v106
	s_nop 1
	v_mov_b32_e32 v10, vcc_lo
	v_mov_b32_e32 v11, vcc_hi
	v_cmp_ne_u32_e32 vcc, 0, v107
	v_cndmask_b32_e64 v2, v2, v10, s[16:17]
	v_cndmask_b32_e64 v8, v9, v11, s[16:17]
	v_mov_b32_e32 v9, vcc_hi
	v_mov_b32_e32 v10, vcc_lo
	v_cndmask_b32_e64 v9, v8, v9, s[18:19]
	v_cndmask_b32_e64 v8, v2, v10, s[18:19]
	s_mov_b64 s[2:3], exec
	s_mov_b64 exec, s[0:1]
	global_store_dwordx2 v[4:5], v[8:9], off
	s_mov_b64 exec, s[2:3]
	v_cmp_ne_u64_e32 vcc, 0, v[8:9]
	s_and_b64 s[20:21], s[0:1], vcc
	s_cmp_lg_u64 s[20:21], 0
	s_cselect_b32 s20, 1, 0
	s_or_b32 s76, s76, s20
	v_cmp_ne_u64_e32 vcc, -1, v[8:9]
	s_and_b64 s[20:21], s[0:1], vcc
	s_cmp_lg_u64 s[20:21], 0
	s_cselect_b32 s20, 1, 0
	s_or_b32 s77, s77, s20
	v_lshl_add_u64 v[4:5], v[4:5], 0, 8
	global_load_dword v156, v96, s[60:61] offset:1792 nt
	global_load_dword v157, v96, s[62:63] offset:1792 nt
	global_load_dword v158, v96, s[64:65] offset:1792 nt
	global_load_dword v159, v96, s[66:67] offset:1792 nt
	global_load_dword v160, v96, s[68:69] offset:1792 nt
	global_load_dword v161, v96, s[70:71] offset:1792 nt
	global_load_dword v162, v96, s[72:73] offset:1792 nt
	global_load_dword v163, v96, s[74:75] offset:1792 nt
	s_waitcnt vmcnt(49)
	v_cmp_ne_u32_e32 vcc, 0, v108
	s_nop 1
	v_mov_b32_e32 v2, vcc_lo
	v_mov_b32_e32 v9, vcc_hi
	v_cmp_ne_u32_e32 vcc, 0, v109
	v_cndmask_b32_e64 v2, 0, v2, s[22:23]
	v_cndmask_b32_e64 v9, 0, v9, s[22:23]
	v_mov_b32_e32 v11, vcc_hi
	v_mov_b32_e32 v14, vcc_lo
	v_cndmask_b32_e64 v9, v9, v11, s[6:7]
	v_cndmask_b32_e64 v2, v2, v14, s[6:7]
	v_cmp_ne_u32_e32 vcc, 0, v110
	s_nop 1
	v_mov_b32_e32 v11, vcc_lo
	v_mov_b32_e32 v14, vcc_hi
	v_cmp_ne_u32_e32 vcc, 0, v111
	v_cndmask_b32_e64 v2, v2, v11, s[8:9]
	v_cndmask_b32_e64 v9, v9, v14, s[8:9]
	v_mov_b32_e32 v11, vcc_hi
	v_mov_b32_e32 v14, vcc_lo
	v_cmp_ne_u32_e32 vcc, 0, v112
	v_cndmask_b32_e64 v9, v9, v11, s[10:11]
	v_cndmask_b32_e64 v2, v2, v14, s[10:11]
	v_mov_b32_e32 v11, vcc_lo
	v_mov_b32_e32 v12, vcc_hi
	v_cmp_ne_u32_e32 vcc, 0, v113
	v_cndmask_b32_e64 v2, v2, v11, s[12:13]
	v_cndmask_b32_e64 v9, v9, v12, s[12:13]
	v_mov_b32_e32 v11, vcc_hi
	v_mov_b32_e32 v12, vcc_lo
	v_cndmask_b32_e64 v9, v9, v11, s[14:15]
	v_cndmask_b32_e64 v2, v2, v12, s[14:15]
	v_cmp_ne_u32_e32 vcc, 0, v114
	s_nop 1
	v_mov_b32_e32 v10, vcc_lo
	v_mov_b32_e32 v11, vcc_hi
	v_cmp_ne_u32_e32 vcc, 0, v115
	v_cndmask_b32_e64 v2, v2, v10, s[16:17]
	v_cndmask_b32_e64 v8, v9, v11, s[16:17]
	v_mov_b32_e32 v9, vcc_hi
	v_mov_b32_e32 v10, vcc_lo
	v_cndmask_b32_e64 v9, v8, v9, s[18:19]
	v_cndmask_b32_e64 v8, v2, v10, s[18:19]
	s_mov_b64 s[2:3], exec
	s_mov_b64 exec, s[0:1]
	global_store_dwordx2 v[4:5], v[8:9], off
	s_mov_b64 exec, s[2:3]
	v_cmp_ne_u64_e32 vcc, 0, v[8:9]
	s_and_b64 s[20:21], s[0:1], vcc
	s_cmp_lg_u64 s[20:21], 0
	s_cselect_b32 s20, 2, 0
	s_or_b32 s76, s76, s20
	v_cmp_ne_u64_e32 vcc, -1, v[8:9]
	s_and_b64 s[20:21], s[0:1], vcc
	s_cmp_lg_u64 s[20:21], 0
	s_cselect_b32 s20, 2, 0
	s_or_b32 s77, s77, s20
	v_lshl_add_u64 v[4:5], v[4:5], 0, 8
	global_load_dword v164, v96, s[60:61] offset:2048 nt
	global_load_dword v165, v96, s[62:63] offset:2048 nt
	global_load_dword v166, v96, s[64:65] offset:2048 nt
	global_load_dword v167, v96, s[66:67] offset:2048 nt
	global_load_dword v168, v96, s[68:69] offset:2048 nt
	global_load_dword v169, v96, s[70:71] offset:2048 nt
	global_load_dword v170, v96, s[72:73] offset:2048 nt
	global_load_dword v171, v96, s[74:75] offset:2048 nt
	s_waitcnt vmcnt(50)
	v_cmp_ne_u32_e32 vcc, 0, v116
	s_nop 1
	v_mov_b32_e32 v2, vcc_lo
	v_mov_b32_e32 v9, vcc_hi
	v_cmp_ne_u32_e32 vcc, 0, v117
	v_cndmask_b32_e64 v2, 0, v2, s[22:23]
	v_cndmask_b32_e64 v9, 0, v9, s[22:23]
	v_mov_b32_e32 v11, vcc_hi
	v_mov_b32_e32 v14, vcc_lo
	v_cndmask_b32_e64 v9, v9, v11, s[6:7]
	v_cndmask_b32_e64 v2, v2, v14, s[6:7]
	v_cmp_ne_u32_e32 vcc, 0, v118
	s_nop 1
	v_mov_b32_e32 v11, vcc_lo
	v_mov_b32_e32 v14, vcc_hi
	v_cmp_ne_u32_e32 vcc, 0, v119
	v_cndmask_b32_e64 v2, v2, v11, s[8:9]
	v_cndmask_b32_e64 v9, v9, v14, s[8:9]
	v_mov_b32_e32 v11, vcc_hi
	v_mov_b32_e32 v14, vcc_lo
	v_cmp_ne_u32_e32 vcc, 0, v120
	v_cndmask_b32_e64 v9, v9, v11, s[10:11]
	v_cndmask_b32_e64 v2, v2, v14, s[10:11]
	v_mov_b32_e32 v11, vcc_lo
	v_mov_b32_e32 v12, vcc_hi
	v_cmp_ne_u32_e32 vcc, 0, v121
	v_cndmask_b32_e64 v2, v2, v11, s[12:13]
	v_cndmask_b32_e64 v9, v9, v12, s[12:13]
	v_mov_b32_e32 v11, vcc_hi
	v_mov_b32_e32 v12, vcc_lo
	v_cndmask_b32_e64 v9, v9, v11, s[14:15]
	v_cndmask_b32_e64 v2, v2, v12, s[14:15]
	v_cmp_ne_u32_e32 vcc, 0, v122
	s_nop 1
	v_mov_b32_e32 v10, vcc_lo
	v_mov_b32_e32 v11, vcc_hi
	v_cmp_ne_u32_e32 vcc, 0, v123
	v_cndmask_b32_e64 v2, v2, v10, s[16:17]
	v_cndmask_b32_e64 v8, v9, v11, s[16:17]
	v_mov_b32_e32 v9, vcc_hi
	v_mov_b32_e32 v10, vcc_lo
	v_cndmask_b32_e64 v9, v8, v9, s[18:19]
	v_cndmask_b32_e64 v8, v2, v10, s[18:19]
	s_mov_b64 s[2:3], exec
	s_mov_b64 exec, s[0:1]
	global_store_dwordx2 v[4:5], v[8:9], off
	s_mov_b64 exec, s[2:3]
	v_cmp_ne_u64_e32 vcc, 0, v[8:9]
	s_and_b64 s[20:21], s[0:1], vcc
	s_cmp_lg_u64 s[20:21], 0
	s_cselect_b32 s20, 4, 0
	s_or_b32 s76, s76, s20
	v_cmp_ne_u64_e32 vcc, -1, v[8:9]
	s_and_b64 s[20:21], s[0:1], vcc
	s_cmp_lg_u64 s[20:21], 0
	s_cselect_b32 s20, 4, 0
	s_or_b32 s77, s77, s20
	v_lshl_add_u64 v[4:5], v[4:5], 0, 8
	global_load_dword v172, v96, s[60:61] offset:2304 nt
	global_load_dword v173, v96, s[62:63] offset:2304 nt
	global_load_dword v174, v96, s[64:65] offset:2304 nt
	global_load_dword v175, v96, s[66:67] offset:2304 nt
	global_load_dword v176, v96, s[68:69] offset:2304 nt
	global_load_dword v177, v96, s[70:71] offset:2304 nt
	global_load_dword v178, v96, s[72:73] offset:2304 nt
	global_load_dword v179, v96, s[74:75] offset:2304 nt
	s_waitcnt vmcnt(51)
	v_cmp_ne_u32_e32 vcc, 0, v124
	s_nop 1
	v_mov_b32_e32 v2, vcc_lo
	v_mov_b32_e32 v9, vcc_hi
	v_cmp_ne_u32_e32 vcc, 0, v125
	v_cndmask_b32_e64 v2, 0, v2, s[22:23]
	v_cndmask_b32_e64 v9, 0, v9, s[22:23]
	v_mov_b32_e32 v11, vcc_hi
	v_mov_b32_e32 v14, vcc_lo
	v_cndmask_b32_e64 v9, v9, v11, s[6:7]
	v_cndmask_b32_e64 v2, v2, v14, s[6:7]
	v_cmp_ne_u32_e32 vcc, 0, v126
	s_nop 1
	v_mov_b32_e32 v11, vcc_lo
	v_mov_b32_e32 v14, vcc_hi
	v_cmp_ne_u32_e32 vcc, 0, v127
	v_cndmask_b32_e64 v2, v2, v11, s[8:9]
	v_cndmask_b32_e64 v9, v9, v14, s[8:9]
	v_mov_b32_e32 v11, vcc_hi
	v_mov_b32_e32 v14, vcc_lo
	v_cmp_ne_u32_e32 vcc, 0, v128
	v_cndmask_b32_e64 v9, v9, v11, s[10:11]
	v_cndmask_b32_e64 v2, v2, v14, s[10:11]
	v_mov_b32_e32 v11, vcc_lo
	v_mov_b32_e32 v12, vcc_hi
	v_cmp_ne_u32_e32 vcc, 0, v129
	v_cndmask_b32_e64 v2, v2, v11, s[12:13]
	v_cndmask_b32_e64 v9, v9, v12, s[12:13]
	v_mov_b32_e32 v11, vcc_hi
	v_mov_b32_e32 v12, vcc_lo
	v_cndmask_b32_e64 v9, v9, v11, s[14:15]
	v_cndmask_b32_e64 v2, v2, v12, s[14:15]
	v_cmp_ne_u32_e32 vcc, 0, v130
	s_nop 1
	v_mov_b32_e32 v10, vcc_lo
	v_mov_b32_e32 v11, vcc_hi
	v_cmp_ne_u32_e32 vcc, 0, v131
	v_cndmask_b32_e64 v2, v2, v10, s[16:17]
	v_cndmask_b32_e64 v8, v9, v11, s[16:17]
	v_mov_b32_e32 v9, vcc_hi
	v_mov_b32_e32 v10, vcc_lo
	v_cndmask_b32_e64 v9, v8, v9, s[18:19]
	v_cndmask_b32_e64 v8, v2, v10, s[18:19]
	s_mov_b64 s[2:3], exec
	s_mov_b64 exec, s[0:1]
	global_store_dwordx2 v[4:5], v[8:9], off
	s_mov_b64 exec, s[2:3]
	v_cmp_ne_u64_e32 vcc, 0, v[8:9]
	s_and_b64 s[20:21], s[0:1], vcc
	s_cmp_lg_u64 s[20:21], 0
	s_cselect_b32 s20, 8, 0
	s_or_b32 s76, s76, s20
	v_cmp_ne_u64_e32 vcc, -1, v[8:9]
	s_and_b64 s[20:21], s[0:1], vcc
	s_cmp_lg_u64 s[20:21], 0
	s_cselect_b32 s20, 8, 0
	s_or_b32 s77, s77, s20
	v_lshl_add_u64 v[4:5], v[4:5], 0, 8
	global_load_dword v180, v96, s[60:61] offset:2560 nt
	global_load_dword v181, v96, s[62:63] offset:2560 nt
	global_load_dword v182, v96, s[64:65] offset:2560 nt
	global_load_dword v183, v96, s[66:67] offset:2560 nt
	global_load_dword v184, v96, s[68:69] offset:2560 nt
	global_load_dword v185, v96, s[70:71] offset:2560 nt
	global_load_dword v186, v96, s[72:73] offset:2560 nt
	global_load_dword v187, v96, s[74:75] offset:2560 nt
	s_waitcnt vmcnt(52)
	v_cmp_ne_u32_e32 vcc, 0, v132
	s_nop 1
	v_mov_b32_e32 v2, vcc_lo
	v_mov_b32_e32 v9, vcc_hi
	v_cmp_ne_u32_e32 vcc, 0, v133
	v_cndmask_b32_e64 v2, 0, v2, s[22:23]
	v_cndmask_b32_e64 v9, 0, v9, s[22:23]
	v_mov_b32_e32 v11, vcc_hi
	v_mov_b32_e32 v14, vcc_lo
	v_cndmask_b32_e64 v9, v9, v11, s[6:7]
	v_cndmask_b32_e64 v2, v2, v14, s[6:7]
	v_cmp_ne_u32_e32 vcc, 0, v134
	s_nop 1
	v_mov_b32_e32 v11, vcc_lo
	v_mov_b32_e32 v14, vcc_hi
	v_cmp_ne_u32_e32 vcc, 0, v135
	v_cndmask_b32_e64 v2, v2, v11, s[8:9]
	v_cndmask_b32_e64 v9, v9, v14, s[8:9]
	v_mov_b32_e32 v11, vcc_hi
	v_mov_b32_e32 v14, vcc_lo
	v_cmp_ne_u32_e32 vcc, 0, v136
	v_cndmask_b32_e64 v9, v9, v11, s[10:11]
	v_cndmask_b32_e64 v2, v2, v14, s[10:11]
	v_mov_b32_e32 v11, vcc_lo
	v_mov_b32_e32 v12, vcc_hi
	v_cmp_ne_u32_e32 vcc, 0, v137
	v_cndmask_b32_e64 v2, v2, v11, s[12:13]
	v_cndmask_b32_e64 v9, v9, v12, s[12:13]
	v_mov_b32_e32 v11, vcc_hi
	v_mov_b32_e32 v12, vcc_lo
	v_cndmask_b32_e64 v9, v9, v11, s[14:15]
	v_cndmask_b32_e64 v2, v2, v12, s[14:15]
	v_cmp_ne_u32_e32 vcc, 0, v138
	s_nop 1
	v_mov_b32_e32 v10, vcc_lo
	v_mov_b32_e32 v11, vcc_hi
	v_cmp_ne_u32_e32 vcc, 0, v139
	v_cndmask_b32_e64 v2, v2, v10, s[16:17]
	v_cndmask_b32_e64 v8, v9, v11, s[16:17]
	v_mov_b32_e32 v9, vcc_hi
	v_mov_b32_e32 v10, vcc_lo
	v_cndmask_b32_e64 v9, v8, v9, s[18:19]
	v_cndmask_b32_e64 v8, v2, v10, s[18:19]
	s_mov_b64 s[2:3], exec
	s_mov_b64 exec, s[0:1]
	global_store_dwordx2 v[4:5], v[8:9], off
	s_mov_b64 exec, s[2:3]
	v_cmp_ne_u64_e32 vcc, 0, v[8:9]
	s_and_b64 s[20:21], s[0:1], vcc
	s_cmp_lg_u64 s[20:21], 0
	s_cselect_b32 s20, 16, 0
	s_or_b32 s76, s76, s20
	v_cmp_ne_u64_e32 vcc, -1, v[8:9]
	s_and_b64 s[20:21], s[0:1], vcc
	s_cmp_lg_u64 s[20:21], 0
	s_cselect_b32 s20, 16, 0
	s_or_b32 s77, s77, s20
	v_lshl_add_u64 v[4:5], v[4:5], 0, 8
	global_load_dword v188, v96, s[60:61] offset:2816 nt
	global_load_dword v189, v96, s[62:63] offset:2816 nt
	global_load_dword v190, v96, s[64:65] offset:2816 nt
	global_load_dword v191, v96, s[66:67] offset:2816 nt
	global_load_dword v192, v96, s[68:69] offset:2816 nt
	global_load_dword v193, v96, s[70:71] offset:2816 nt
	global_load_dword v194, v96, s[72:73] offset:2816 nt
	global_load_dword v195, v96, s[74:75] offset:2816 nt
	s_waitcnt vmcnt(53)
	v_cmp_ne_u32_e32 vcc, 0, v140
	s_nop 1
	v_mov_b32_e32 v2, vcc_lo
	v_mov_b32_e32 v9, vcc_hi
	v_cmp_ne_u32_e32 vcc, 0, v141
	v_cndmask_b32_e64 v2, 0, v2, s[22:23]
	v_cndmask_b32_e64 v9, 0, v9, s[22:23]
	v_mov_b32_e32 v11, vcc_hi
	v_mov_b32_e32 v14, vcc_lo
	v_cndmask_b32_e64 v9, v9, v11, s[6:7]
	v_cndmask_b32_e64 v2, v2, v14, s[6:7]
	v_cmp_ne_u32_e32 vcc, 0, v142
	s_nop 1
	v_mov_b32_e32 v11, vcc_lo
	v_mov_b32_e32 v14, vcc_hi
	v_cmp_ne_u32_e32 vcc, 0, v143
	v_cndmask_b32_e64 v2, v2, v11, s[8:9]
	v_cndmask_b32_e64 v9, v9, v14, s[8:9]
	v_mov_b32_e32 v11, vcc_hi
	v_mov_b32_e32 v14, vcc_lo
	v_cmp_ne_u32_e32 vcc, 0, v144
	v_cndmask_b32_e64 v9, v9, v11, s[10:11]
	v_cndmask_b32_e64 v2, v2, v14, s[10:11]
	v_mov_b32_e32 v11, vcc_lo
	v_mov_b32_e32 v12, vcc_hi
	v_cmp_ne_u32_e32 vcc, 0, v145
	v_cndmask_b32_e64 v2, v2, v11, s[12:13]
	v_cndmask_b32_e64 v9, v9, v12, s[12:13]
	v_mov_b32_e32 v11, vcc_hi
	v_mov_b32_e32 v12, vcc_lo
	v_cndmask_b32_e64 v9, v9, v11, s[14:15]
	v_cndmask_b32_e64 v2, v2, v12, s[14:15]
	v_cmp_ne_u32_e32 vcc, 0, v146
	s_nop 1
	v_mov_b32_e32 v10, vcc_lo
	v_mov_b32_e32 v11, vcc_hi
	v_cmp_ne_u32_e32 vcc, 0, v147
	v_cndmask_b32_e64 v2, v2, v10, s[16:17]
	v_cndmask_b32_e64 v8, v9, v11, s[16:17]
	v_mov_b32_e32 v9, vcc_hi
	v_mov_b32_e32 v10, vcc_lo
	v_cndmask_b32_e64 v9, v8, v9, s[18:19]
	v_cndmask_b32_e64 v8, v2, v10, s[18:19]
	s_mov_b64 s[2:3], exec
	s_mov_b64 exec, s[0:1]
	global_store_dwordx2 v[4:5], v[8:9], off
	s_mov_b64 exec, s[2:3]
	v_cmp_ne_u64_e32 vcc, 0, v[8:9]
	s_and_b64 s[20:21], s[0:1], vcc
	s_cmp_lg_u64 s[20:21], 0
	s_cselect_b32 s20, 32, 0
	s_or_b32 s76, s76, s20
	v_cmp_ne_u64_e32 vcc, -1, v[8:9]
	s_and_b64 s[20:21], s[0:1], vcc
	s_cmp_lg_u64 s[20:21], 0
	s_cselect_b32 s20, 32, 0
	s_or_b32 s77, s77, s20
	v_lshl_add_u64 v[4:5], v[4:5], 0, 8
	global_load_dword v196, v96, s[60:61] offset:3072 nt
	global_load_dword v197, v96, s[62:63] offset:3072 nt
	global_load_dword v198, v96, s[64:65] offset:3072 nt
	global_load_dword v199, v96, s[66:67] offset:3072 nt
	global_load_dword v200, v96, s[68:69] offset:3072 nt
	global_load_dword v201, v96, s[70:71] offset:3072 nt
	global_load_dword v202, v96, s[72:73] offset:3072 nt
	global_load_dword v203, v96, s[74:75] offset:3072 nt
	s_waitcnt vmcnt(54)
	v_cmp_ne_u32_e32 vcc, 0, v148
	s_nop 1
	v_mov_b32_e32 v2, vcc_lo
	v_mov_b32_e32 v9, vcc_hi
	v_cmp_ne_u32_e32 vcc, 0, v149
	v_cndmask_b32_e64 v2, 0, v2, s[22:23]
	v_cndmask_b32_e64 v9, 0, v9, s[22:23]
	v_mov_b32_e32 v11, vcc_hi
	v_mov_b32_e32 v14, vcc_lo
	v_cndmask_b32_e64 v9, v9, v11, s[6:7]
	v_cndmask_b32_e64 v2, v2, v14, s[6:7]
	v_cmp_ne_u32_e32 vcc, 0, v150
	s_nop 1
	v_mov_b32_e32 v11, vcc_lo
	v_mov_b32_e32 v14, vcc_hi
	v_cmp_ne_u32_e32 vcc, 0, v151
	v_cndmask_b32_e64 v2, v2, v11, s[8:9]
	v_cndmask_b32_e64 v9, v9, v14, s[8:9]
	v_mov_b32_e32 v11, vcc_hi
	v_mov_b32_e32 v14, vcc_lo
	v_cmp_ne_u32_e32 vcc, 0, v152
	v_cndmask_b32_e64 v9, v9, v11, s[10:11]
	v_cndmask_b32_e64 v2, v2, v14, s[10:11]
	v_mov_b32_e32 v11, vcc_lo
	v_mov_b32_e32 v12, vcc_hi
	v_cmp_ne_u32_e32 vcc, 0, v153
	v_cndmask_b32_e64 v2, v2, v11, s[12:13]
	v_cndmask_b32_e64 v9, v9, v12, s[12:13]
	v_mov_b32_e32 v11, vcc_hi
	v_mov_b32_e32 v12, vcc_lo
	v_cndmask_b32_e64 v9, v9, v11, s[14:15]
	v_cndmask_b32_e64 v2, v2, v12, s[14:15]
	v_cmp_ne_u32_e32 vcc, 0, v154
	s_nop 1
	v_mov_b32_e32 v10, vcc_lo
	v_mov_b32_e32 v11, vcc_hi
	v_cmp_ne_u32_e32 vcc, 0, v155
	v_cndmask_b32_e64 v2, v2, v10, s[16:17]
	v_cndmask_b32_e64 v8, v9, v11, s[16:17]
	v_mov_b32_e32 v9, vcc_hi
	v_mov_b32_e32 v10, vcc_lo
	v_cndmask_b32_e64 v9, v8, v9, s[18:19]
	v_cndmask_b32_e64 v8, v2, v10, s[18:19]
	s_mov_b64 s[2:3], exec
	s_mov_b64 exec, s[0:1]
	global_store_dwordx2 v[4:5], v[8:9], off
	s_mov_b64 exec, s[2:3]
	v_cmp_ne_u64_e32 vcc, 0, v[8:9]
	s_and_b64 s[20:21], s[0:1], vcc
	s_cmp_lg_u64 s[20:21], 0
	s_cselect_b32 s20, 64, 0
	s_or_b32 s76, s76, s20
	v_cmp_ne_u64_e32 vcc, -1, v[8:9]
	s_and_b64 s[20:21], s[0:1], vcc
	s_cmp_lg_u64 s[20:21], 0
	s_cselect_b32 s20, 64, 0
	s_or_b32 s77, s77, s20
	v_lshl_add_u64 v[4:5], v[4:5], 0, 8
	global_load_dword v204, v96, s[60:61] offset:3328 nt
	global_load_dword v205, v96, s[62:63] offset:3328 nt
	global_load_dword v206, v96, s[64:65] offset:3328 nt
	global_load_dword v207, v96, s[66:67] offset:3328 nt
	global_load_dword v208, v96, s[68:69] offset:3328 nt
	global_load_dword v209, v96, s[70:71] offset:3328 nt
	global_load_dword v210, v96, s[72:73] offset:3328 nt
	global_load_dword v211, v96, s[74:75] offset:3328 nt
	s_waitcnt vmcnt(54)
	v_cmp_ne_u32_e32 vcc, 0, v156
	s_nop 1
	v_mov_b32_e32 v2, vcc_lo
	v_mov_b32_e32 v9, vcc_hi
	v_cmp_ne_u32_e32 vcc, 0, v157
	v_cndmask_b32_e64 v2, 0, v2, s[22:23]
	v_cndmask_b32_e64 v9, 0, v9, s[22:23]
	v_mov_b32_e32 v11, vcc_hi
	v_mov_b32_e32 v14, vcc_lo
	v_cndmask_b32_e64 v9, v9, v11, s[6:7]
	v_cndmask_b32_e64 v2, v2, v14, s[6:7]
	v_cmp_ne_u32_e32 vcc, 0, v158
	s_nop 1
	v_mov_b32_e32 v11, vcc_lo
	v_mov_b32_e32 v14, vcc_hi
	v_cmp_ne_u32_e32 vcc, 0, v159
	v_cndmask_b32_e64 v2, v2, v11, s[8:9]
	v_cndmask_b32_e64 v9, v9, v14, s[8:9]
	v_mov_b32_e32 v11, vcc_hi
	v_mov_b32_e32 v14, vcc_lo
	v_cmp_ne_u32_e32 vcc, 0, v160
	v_cndmask_b32_e64 v9, v9, v11, s[10:11]
	v_cndmask_b32_e64 v2, v2, v14, s[10:11]
	v_mov_b32_e32 v11, vcc_lo
	v_mov_b32_e32 v12, vcc_hi
	v_cmp_ne_u32_e32 vcc, 0, v161
	v_cndmask_b32_e64 v2, v2, v11, s[12:13]
	v_cndmask_b32_e64 v9, v9, v12, s[12:13]
	v_mov_b32_e32 v11, vcc_hi
	v_mov_b32_e32 v12, vcc_lo
	v_cndmask_b32_e64 v9, v9, v11, s[14:15]
	v_cndmask_b32_e64 v2, v2, v12, s[14:15]
	v_cmp_ne_u32_e32 vcc, 0, v162
	s_nop 1
	v_mov_b32_e32 v10, vcc_lo
	v_mov_b32_e32 v11, vcc_hi
	v_cmp_ne_u32_e32 vcc, 0, v163
	v_cndmask_b32_e64 v2, v2, v10, s[16:17]
	v_cndmask_b32_e64 v8, v9, v11, s[16:17]
	v_mov_b32_e32 v9, vcc_hi
	v_mov_b32_e32 v10, vcc_lo
	v_cndmask_b32_e64 v9, v8, v9, s[18:19]
	v_cndmask_b32_e64 v8, v2, v10, s[18:19]
	s_mov_b64 s[2:3], exec
	s_mov_b64 exec, s[0:1]
	global_store_dwordx2 v[4:5], v[8:9], off
	s_mov_b64 exec, s[2:3]
	v_cmp_ne_u64_e32 vcc, 0, v[8:9]
	s_and_b64 s[20:21], s[0:1], vcc
	s_cmp_lg_u64 s[20:21], 0
	s_cselect_b32 s20, 128, 0
	s_or_b32 s76, s76, s20
	v_cmp_ne_u64_e32 vcc, -1, v[8:9]
	s_and_b64 s[20:21], s[0:1], vcc
	s_cmp_lg_u64 s[20:21], 0
	s_cselect_b32 s20, 128, 0
	s_or_b32 s77, s77, s20
	v_lshl_add_u64 v[4:5], v[4:5], 0, 8
	global_load_dword v212, v96, s[60:61] offset:3584 nt
	global_load_dword v213, v96, s[62:63] offset:3584 nt
	global_load_dword v214, v96, s[64:65] offset:3584 nt
	global_load_dword v215, v96, s[66:67] offset:3584 nt
	global_load_dword v216, v96, s[68:69] offset:3584 nt
	global_load_dword v217, v96, s[70:71] offset:3584 nt
	global_load_dword v218, v96, s[72:73] offset:3584 nt
	global_load_dword v219, v96, s[74:75] offset:3584 nt
	s_waitcnt vmcnt(54)
	v_cmp_ne_u32_e32 vcc, 0, v164
	s_nop 1
	v_mov_b32_e32 v2, vcc_lo
	v_mov_b32_e32 v9, vcc_hi
	v_cmp_ne_u32_e32 vcc, 0, v165
	v_cndmask_b32_e64 v2, 0, v2, s[22:23]
	v_cndmask_b32_e64 v9, 0, v9, s[22:23]
	v_mov_b32_e32 v11, vcc_hi
	v_mov_b32_e32 v14, vcc_lo
	v_cndmask_b32_e64 v9, v9, v11, s[6:7]
	v_cndmask_b32_e64 v2, v2, v14, s[6:7]
	v_cmp_ne_u32_e32 vcc, 0, v166
	s_nop 1
	v_mov_b32_e32 v11, vcc_lo
	v_mov_b32_e32 v14, vcc_hi
	v_cmp_ne_u32_e32 vcc, 0, v167
	v_cndmask_b32_e64 v2, v2, v11, s[8:9]
	v_cndmask_b32_e64 v9, v9, v14, s[8:9]
	v_mov_b32_e32 v11, vcc_hi
	v_mov_b32_e32 v14, vcc_lo
	v_cmp_ne_u32_e32 vcc, 0, v168
	v_cndmask_b32_e64 v9, v9, v11, s[10:11]
	v_cndmask_b32_e64 v2, v2, v14, s[10:11]
	v_mov_b32_e32 v11, vcc_lo
	v_mov_b32_e32 v12, vcc_hi
	v_cmp_ne_u32_e32 vcc, 0, v169
	v_cndmask_b32_e64 v2, v2, v11, s[12:13]
	v_cndmask_b32_e64 v9, v9, v12, s[12:13]
	v_mov_b32_e32 v11, vcc_hi
	v_mov_b32_e32 v12, vcc_lo
	v_cndmask_b32_e64 v9, v9, v11, s[14:15]
	v_cndmask_b32_e64 v2, v2, v12, s[14:15]
	v_cmp_ne_u32_e32 vcc, 0, v170
	s_nop 1
	v_mov_b32_e32 v10, vcc_lo
	v_mov_b32_e32 v11, vcc_hi
	v_cmp_ne_u32_e32 vcc, 0, v171
	v_cndmask_b32_e64 v2, v2, v10, s[16:17]
	v_cndmask_b32_e64 v8, v9, v11, s[16:17]
	v_mov_b32_e32 v9, vcc_hi
	v_mov_b32_e32 v10, vcc_lo
	v_cndmask_b32_e64 v9, v8, v9, s[18:19]
	v_cndmask_b32_e64 v8, v2, v10, s[18:19]
	s_mov_b64 s[2:3], exec
	s_mov_b64 exec, s[0:1]
	global_store_dwordx2 v[4:5], v[8:9], off
	s_mov_b64 exec, s[2:3]
	v_cmp_ne_u64_e32 vcc, 0, v[8:9]
	s_and_b64 s[20:21], s[0:1], vcc
	s_cmp_lg_u64 s[20:21], 0
	s_cselect_b32 s20, 256, 0
	s_or_b32 s76, s76, s20
	v_cmp_ne_u64_e32 vcc, -1, v[8:9]
	s_and_b64 s[20:21], s[0:1], vcc
	s_cmp_lg_u64 s[20:21], 0
	s_cselect_b32 s20, 256, 0
	s_or_b32 s77, s77, s20
	v_lshl_add_u64 v[4:5], v[4:5], 0, 8
	global_load_dword v220, v96, s[60:61] offset:3840 nt
	global_load_dword v221, v96, s[62:63] offset:3840 nt
	global_load_dword v222, v96, s[64:65] offset:3840 nt
	global_load_dword v223, v96, s[66:67] offset:3840 nt
	global_load_dword v224, v96, s[68:69] offset:3840 nt
	global_load_dword v225, v96, s[70:71] offset:3840 nt
	global_load_dword v226, v96, s[72:73] offset:3840 nt
	global_load_dword v227, v96, s[74:75] offset:3840 nt
	s_waitcnt vmcnt(54)
	v_cmp_ne_u32_e32 vcc, 0, v172
	s_nop 1
	v_mov_b32_e32 v2, vcc_lo
	v_mov_b32_e32 v9, vcc_hi
	v_cmp_ne_u32_e32 vcc, 0, v173
	v_cndmask_b32_e64 v2, 0, v2, s[22:23]
	v_cndmask_b32_e64 v9, 0, v9, s[22:23]
	v_mov_b32_e32 v11, vcc_hi
	v_mov_b32_e32 v14, vcc_lo
	v_cndmask_b32_e64 v9, v9, v11, s[6:7]
	v_cndmask_b32_e64 v2, v2, v14, s[6:7]
	v_cmp_ne_u32_e32 vcc, 0, v174
	s_nop 1
	v_mov_b32_e32 v11, vcc_lo
	v_mov_b32_e32 v14, vcc_hi
	v_cmp_ne_u32_e32 vcc, 0, v175
	v_cndmask_b32_e64 v2, v2, v11, s[8:9]
	v_cndmask_b32_e64 v9, v9, v14, s[8:9]
	v_mov_b32_e32 v11, vcc_hi
	v_mov_b32_e32 v14, vcc_lo
	v_cmp_ne_u32_e32 vcc, 0, v176
	v_cndmask_b32_e64 v9, v9, v11, s[10:11]
	v_cndmask_b32_e64 v2, v2, v14, s[10:11]
	v_mov_b32_e32 v11, vcc_lo
	v_mov_b32_e32 v12, vcc_hi
	v_cmp_ne_u32_e32 vcc, 0, v177
	v_cndmask_b32_e64 v2, v2, v11, s[12:13]
	v_cndmask_b32_e64 v9, v9, v12, s[12:13]
	v_mov_b32_e32 v11, vcc_hi
	v_mov_b32_e32 v12, vcc_lo
	v_cndmask_b32_e64 v9, v9, v11, s[14:15]
	v_cndmask_b32_e64 v2, v2, v12, s[14:15]
	v_cmp_ne_u32_e32 vcc, 0, v178
	s_nop 1
	v_mov_b32_e32 v10, vcc_lo
	v_mov_b32_e32 v11, vcc_hi
	v_cmp_ne_u32_e32 vcc, 0, v179
	v_cndmask_b32_e64 v2, v2, v10, s[16:17]
	v_cndmask_b32_e64 v8, v9, v11, s[16:17]
	v_mov_b32_e32 v9, vcc_hi
	v_mov_b32_e32 v10, vcc_lo
	v_cndmask_b32_e64 v9, v8, v9, s[18:19]
	v_cndmask_b32_e64 v8, v2, v10, s[18:19]
	s_mov_b64 s[2:3], exec
	s_mov_b64 exec, s[0:1]
	global_store_dwordx2 v[4:5], v[8:9], off
	s_mov_b64 exec, s[2:3]
	v_cmp_ne_u64_e32 vcc, 0, v[8:9]
	s_and_b64 s[20:21], s[0:1], vcc
	s_cmp_lg_u64 s[20:21], 0
	s_cselect_b32 s20, 512, 0
	s_or_b32 s76, s76, s20
	v_cmp_ne_u64_e32 vcc, -1, v[8:9]
	s_and_b64 s[20:21], s[0:1], vcc
	s_cmp_lg_u64 s[20:21], 0
	s_cselect_b32 s20, 512, 0
	s_or_b32 s77, s77, s20
	v_lshl_add_u64 v[4:5], v[4:5], 0, 8
	s_waitcnt vmcnt(46)
	v_cmp_ne_u32_e32 vcc, 0, v180
	s_nop 1
	v_mov_b32_e32 v2, vcc_lo
	v_mov_b32_e32 v9, vcc_hi
	v_cmp_ne_u32_e32 vcc, 0, v181
	v_cndmask_b32_e64 v2, 0, v2, s[22:23]
	v_cndmask_b32_e64 v9, 0, v9, s[22:23]
	v_mov_b32_e32 v11, vcc_hi
	v_mov_b32_e32 v14, vcc_lo
	v_cndmask_b32_e64 v9, v9, v11, s[6:7]
	v_cndmask_b32_e64 v2, v2, v14, s[6:7]
	v_cmp_ne_u32_e32 vcc, 0, v182
	s_nop 1
	v_mov_b32_e32 v11, vcc_lo
	v_mov_b32_e32 v14, vcc_hi
	v_cmp_ne_u32_e32 vcc, 0, v183
	v_cndmask_b32_e64 v2, v2, v11, s[8:9]
	v_cndmask_b32_e64 v9, v9, v14, s[8:9]
	v_mov_b32_e32 v11, vcc_hi
	v_mov_b32_e32 v14, vcc_lo
	v_cmp_ne_u32_e32 vcc, 0, v184
	v_cndmask_b32_e64 v9, v9, v11, s[10:11]
	v_cndmask_b32_e64 v2, v2, v14, s[10:11]
	v_mov_b32_e32 v11, vcc_lo
	v_mov_b32_e32 v12, vcc_hi
	v_cmp_ne_u32_e32 vcc, 0, v185
	v_cndmask_b32_e64 v2, v2, v11, s[12:13]
	v_cndmask_b32_e64 v9, v9, v12, s[12:13]
	v_mov_b32_e32 v11, vcc_hi
	v_mov_b32_e32 v12, vcc_lo
	v_cndmask_b32_e64 v9, v9, v11, s[14:15]
	v_cndmask_b32_e64 v2, v2, v12, s[14:15]
	v_cmp_ne_u32_e32 vcc, 0, v186
	s_nop 1
	v_mov_b32_e32 v10, vcc_lo
	v_mov_b32_e32 v11, vcc_hi
	v_cmp_ne_u32_e32 vcc, 0, v187
	v_cndmask_b32_e64 v2, v2, v10, s[16:17]
	v_cndmask_b32_e64 v8, v9, v11, s[16:17]
	v_mov_b32_e32 v9, vcc_hi
	v_mov_b32_e32 v10, vcc_lo
	v_cndmask_b32_e64 v9, v8, v9, s[18:19]
	v_cndmask_b32_e64 v8, v2, v10, s[18:19]
	s_mov_b64 s[2:3], exec
	s_mov_b64 exec, s[0:1]
	global_store_dwordx2 v[4:5], v[8:9], off
	s_mov_b64 exec, s[2:3]
	v_cmp_ne_u64_e32 vcc, 0, v[8:9]
	s_and_b64 s[20:21], s[0:1], vcc
	s_cmp_lg_u64 s[20:21], 0
	s_cselect_b32 s20, 1024, 0
	s_or_b32 s76, s76, s20
	v_cmp_ne_u64_e32 vcc, -1, v[8:9]
	s_and_b64 s[20:21], s[0:1], vcc
	s_cmp_lg_u64 s[20:21], 0
	s_cselect_b32 s20, 1024, 0
	s_or_b32 s77, s77, s20
	v_lshl_add_u64 v[4:5], v[4:5], 0, 8
	s_waitcnt vmcnt(38)
	v_cmp_ne_u32_e32 vcc, 0, v188
	s_nop 1
	v_mov_b32_e32 v2, vcc_lo
	v_mov_b32_e32 v9, vcc_hi
	v_cmp_ne_u32_e32 vcc, 0, v189
	v_cndmask_b32_e64 v2, 0, v2, s[22:23]
	v_cndmask_b32_e64 v9, 0, v9, s[22:23]
	v_mov_b32_e32 v11, vcc_hi
	v_mov_b32_e32 v14, vcc_lo
	v_cndmask_b32_e64 v9, v9, v11, s[6:7]
	v_cndmask_b32_e64 v2, v2, v14, s[6:7]
	v_cmp_ne_u32_e32 vcc, 0, v190
	s_nop 1
	v_mov_b32_e32 v11, vcc_lo
	v_mov_b32_e32 v14, vcc_hi
	v_cmp_ne_u32_e32 vcc, 0, v191
	v_cndmask_b32_e64 v2, v2, v11, s[8:9]
	v_cndmask_b32_e64 v9, v9, v14, s[8:9]
	v_mov_b32_e32 v11, vcc_hi
	v_mov_b32_e32 v14, vcc_lo
	v_cmp_ne_u32_e32 vcc, 0, v192
	v_cndmask_b32_e64 v9, v9, v11, s[10:11]
	v_cndmask_b32_e64 v2, v2, v14, s[10:11]
	v_mov_b32_e32 v11, vcc_lo
	v_mov_b32_e32 v12, vcc_hi
	v_cmp_ne_u32_e32 vcc, 0, v193
	v_cndmask_b32_e64 v2, v2, v11, s[12:13]
	v_cndmask_b32_e64 v9, v9, v12, s[12:13]
	v_mov_b32_e32 v11, vcc_hi
	v_mov_b32_e32 v12, vcc_lo
	v_cndmask_b32_e64 v9, v9, v11, s[14:15]
	v_cndmask_b32_e64 v2, v2, v12, s[14:15]
	v_cmp_ne_u32_e32 vcc, 0, v194
	s_nop 1
	v_mov_b32_e32 v10, vcc_lo
	v_mov_b32_e32 v11, vcc_hi
	v_cmp_ne_u32_e32 vcc, 0, v195
	v_cndmask_b32_e64 v2, v2, v10, s[16:17]
	v_cndmask_b32_e64 v8, v9, v11, s[16:17]
	v_mov_b32_e32 v9, vcc_hi
	v_mov_b32_e32 v10, vcc_lo
	v_cndmask_b32_e64 v9, v8, v9, s[18:19]
	v_cndmask_b32_e64 v8, v2, v10, s[18:19]
	s_mov_b64 s[2:3], exec
	s_mov_b64 exec, s[0:1]
	global_store_dwordx2 v[4:5], v[8:9], off
	s_mov_b64 exec, s[2:3]
	v_cmp_ne_u64_e32 vcc, 0, v[8:9]
	s_and_b64 s[20:21], s[0:1], vcc
	s_cmp_lg_u64 s[20:21], 0
	s_cselect_b32 s20, 2048, 0
	s_or_b32 s76, s76, s20
	v_cmp_ne_u64_e32 vcc, -1, v[8:9]
	s_and_b64 s[20:21], s[0:1], vcc
	s_cmp_lg_u64 s[20:21], 0
	s_cselect_b32 s20, 2048, 0
	s_or_b32 s77, s77, s20
	v_lshl_add_u64 v[4:5], v[4:5], 0, 8
	s_waitcnt vmcnt(30)
	v_cmp_ne_u32_e32 vcc, 0, v196
	s_nop 1
	v_mov_b32_e32 v2, vcc_lo
	v_mov_b32_e32 v9, vcc_hi
	v_cmp_ne_u32_e32 vcc, 0, v197
	v_cndmask_b32_e64 v2, 0, v2, s[22:23]
	v_cndmask_b32_e64 v9, 0, v9, s[22:23]
	v_mov_b32_e32 v11, vcc_hi
	v_mov_b32_e32 v14, vcc_lo
	v_cndmask_b32_e64 v9, v9, v11, s[6:7]
	v_cndmask_b32_e64 v2, v2, v14, s[6:7]
	v_cmp_ne_u32_e32 vcc, 0, v198
	s_nop 1
	v_mov_b32_e32 v11, vcc_lo
	v_mov_b32_e32 v14, vcc_hi
	v_cmp_ne_u32_e32 vcc, 0, v199
	v_cndmask_b32_e64 v2, v2, v11, s[8:9]
	v_cndmask_b32_e64 v9, v9, v14, s[8:9]
	v_mov_b32_e32 v11, vcc_hi
	v_mov_b32_e32 v14, vcc_lo
	v_cmp_ne_u32_e32 vcc, 0, v200
	v_cndmask_b32_e64 v9, v9, v11, s[10:11]
	v_cndmask_b32_e64 v2, v2, v14, s[10:11]
	v_mov_b32_e32 v11, vcc_lo
	v_mov_b32_e32 v12, vcc_hi
	v_cmp_ne_u32_e32 vcc, 0, v201
	v_cndmask_b32_e64 v2, v2, v11, s[12:13]
	v_cndmask_b32_e64 v9, v9, v12, s[12:13]
	v_mov_b32_e32 v11, vcc_hi
	v_mov_b32_e32 v12, vcc_lo
	v_cndmask_b32_e64 v9, v9, v11, s[14:15]
	v_cndmask_b32_e64 v2, v2, v12, s[14:15]
	v_cmp_ne_u32_e32 vcc, 0, v202
	s_nop 1
	v_mov_b32_e32 v10, vcc_lo
	v_mov_b32_e32 v11, vcc_hi
	v_cmp_ne_u32_e32 vcc, 0, v203
	v_cndmask_b32_e64 v2, v2, v10, s[16:17]
	v_cndmask_b32_e64 v8, v9, v11, s[16:17]
	v_mov_b32_e32 v9, vcc_hi
	v_mov_b32_e32 v10, vcc_lo
	v_cndmask_b32_e64 v9, v8, v9, s[18:19]
	v_cndmask_b32_e64 v8, v2, v10, s[18:19]
	s_mov_b64 s[2:3], exec
	s_mov_b64 exec, s[0:1]
	global_store_dwordx2 v[4:5], v[8:9], off
	s_mov_b64 exec, s[2:3]
	v_cmp_ne_u64_e32 vcc, 0, v[8:9]
	s_and_b64 s[20:21], s[0:1], vcc
	s_cmp_lg_u64 s[20:21], 0
	s_cselect_b32 s20, 4096, 0
	s_or_b32 s76, s76, s20
	v_cmp_ne_u64_e32 vcc, -1, v[8:9]
	s_and_b64 s[20:21], s[0:1], vcc
	s_cmp_lg_u64 s[20:21], 0
	s_cselect_b32 s20, 4096, 0
	s_or_b32 s77, s77, s20
	v_lshl_add_u64 v[4:5], v[4:5], 0, 8
	s_waitcnt vmcnt(22)
	v_cmp_ne_u32_e32 vcc, 0, v204
	s_nop 1
	v_mov_b32_e32 v2, vcc_lo
	v_mov_b32_e32 v9, vcc_hi
	v_cmp_ne_u32_e32 vcc, 0, v205
	v_cndmask_b32_e64 v2, 0, v2, s[22:23]
	v_cndmask_b32_e64 v9, 0, v9, s[22:23]
	v_mov_b32_e32 v11, vcc_hi
	v_mov_b32_e32 v14, vcc_lo
	v_cndmask_b32_e64 v9, v9, v11, s[6:7]
	v_cndmask_b32_e64 v2, v2, v14, s[6:7]
	v_cmp_ne_u32_e32 vcc, 0, v206
	s_nop 1
	v_mov_b32_e32 v11, vcc_lo
	v_mov_b32_e32 v14, vcc_hi
	v_cmp_ne_u32_e32 vcc, 0, v207
	v_cndmask_b32_e64 v2, v2, v11, s[8:9]
	v_cndmask_b32_e64 v9, v9, v14, s[8:9]
	v_mov_b32_e32 v11, vcc_hi
	v_mov_b32_e32 v14, vcc_lo
	v_cmp_ne_u32_e32 vcc, 0, v208
	v_cndmask_b32_e64 v9, v9, v11, s[10:11]
	v_cndmask_b32_e64 v2, v2, v14, s[10:11]
	v_mov_b32_e32 v11, vcc_lo
	v_mov_b32_e32 v12, vcc_hi
	v_cmp_ne_u32_e32 vcc, 0, v209
	v_cndmask_b32_e64 v2, v2, v11, s[12:13]
	v_cndmask_b32_e64 v9, v9, v12, s[12:13]
	v_mov_b32_e32 v11, vcc_hi
	v_mov_b32_e32 v12, vcc_lo
	v_cndmask_b32_e64 v9, v9, v11, s[14:15]
	v_cndmask_b32_e64 v2, v2, v12, s[14:15]
	v_cmp_ne_u32_e32 vcc, 0, v210
	s_nop 1
	v_mov_b32_e32 v10, vcc_lo
	v_mov_b32_e32 v11, vcc_hi
	v_cmp_ne_u32_e32 vcc, 0, v211
	v_cndmask_b32_e64 v2, v2, v10, s[16:17]
	v_cndmask_b32_e64 v8, v9, v11, s[16:17]
	v_mov_b32_e32 v9, vcc_hi
	v_mov_b32_e32 v10, vcc_lo
	v_cndmask_b32_e64 v9, v8, v9, s[18:19]
	v_cndmask_b32_e64 v8, v2, v10, s[18:19]
	s_mov_b64 s[2:3], exec
	s_mov_b64 exec, s[0:1]
	global_store_dwordx2 v[4:5], v[8:9], off
	s_mov_b64 exec, s[2:3]
	v_cmp_ne_u64_e32 vcc, 0, v[8:9]
	s_and_b64 s[20:21], s[0:1], vcc
	s_cmp_lg_u64 s[20:21], 0
	s_cselect_b32 s20, 8192, 0
	s_or_b32 s76, s76, s20
	v_cmp_ne_u64_e32 vcc, -1, v[8:9]
	s_and_b64 s[20:21], s[0:1], vcc
	s_cmp_lg_u64 s[20:21], 0
	s_cselect_b32 s20, 8192, 0
	s_or_b32 s77, s77, s20
	v_lshl_add_u64 v[4:5], v[4:5], 0, 8
	s_waitcnt vmcnt(14)
	v_cmp_ne_u32_e32 vcc, 0, v212
	s_nop 1
	v_mov_b32_e32 v2, vcc_lo
	v_mov_b32_e32 v9, vcc_hi
	v_cmp_ne_u32_e32 vcc, 0, v213
	v_cndmask_b32_e64 v2, 0, v2, s[22:23]
	v_cndmask_b32_e64 v9, 0, v9, s[22:23]
	v_mov_b32_e32 v11, vcc_hi
	v_mov_b32_e32 v14, vcc_lo
	v_cndmask_b32_e64 v9, v9, v11, s[6:7]
	v_cndmask_b32_e64 v2, v2, v14, s[6:7]
	v_cmp_ne_u32_e32 vcc, 0, v214
	s_nop 1
	v_mov_b32_e32 v11, vcc_lo
	v_mov_b32_e32 v14, vcc_hi
	v_cmp_ne_u32_e32 vcc, 0, v215
	v_cndmask_b32_e64 v2, v2, v11, s[8:9]
	v_cndmask_b32_e64 v9, v9, v14, s[8:9]
	v_mov_b32_e32 v11, vcc_hi
	v_mov_b32_e32 v14, vcc_lo
	v_cmp_ne_u32_e32 vcc, 0, v216
	v_cndmask_b32_e64 v9, v9, v11, s[10:11]
	v_cndmask_b32_e64 v2, v2, v14, s[10:11]
	v_mov_b32_e32 v11, vcc_lo
	v_mov_b32_e32 v12, vcc_hi
	v_cmp_ne_u32_e32 vcc, 0, v217
	v_cndmask_b32_e64 v2, v2, v11, s[12:13]
	v_cndmask_b32_e64 v9, v9, v12, s[12:13]
	v_mov_b32_e32 v11, vcc_hi
	v_mov_b32_e32 v12, vcc_lo
	v_cndmask_b32_e64 v9, v9, v11, s[14:15]
	v_cndmask_b32_e64 v2, v2, v12, s[14:15]
	v_cmp_ne_u32_e32 vcc, 0, v218
	s_nop 1
	v_mov_b32_e32 v10, vcc_lo
	v_mov_b32_e32 v11, vcc_hi
	v_cmp_ne_u32_e32 vcc, 0, v219
	v_cndmask_b32_e64 v2, v2, v10, s[16:17]
	v_cndmask_b32_e64 v8, v9, v11, s[16:17]
	v_mov_b32_e32 v9, vcc_hi
	v_mov_b32_e32 v10, vcc_lo
	v_cndmask_b32_e64 v9, v8, v9, s[18:19]
	v_cndmask_b32_e64 v8, v2, v10, s[18:19]
	s_mov_b64 s[2:3], exec
	s_mov_b64 exec, s[0:1]
	global_store_dwordx2 v[4:5], v[8:9], off
	s_mov_b64 exec, s[2:3]
	v_cmp_ne_u64_e32 vcc, 0, v[8:9]
	s_and_b64 s[20:21], s[0:1], vcc
	s_cmp_lg_u64 s[20:21], 0
	s_cselect_b32 s20, 16384, 0
	s_or_b32 s76, s76, s20
	v_cmp_ne_u64_e32 vcc, -1, v[8:9]
	s_and_b64 s[20:21], s[0:1], vcc
	s_cmp_lg_u64 s[20:21], 0
	s_cselect_b32 s20, 16384, 0
	s_or_b32 s77, s77, s20
	v_lshl_add_u64 v[4:5], v[4:5], 0, 8
	s_waitcnt vmcnt(6)
	v_cmp_ne_u32_e32 vcc, 0, v220
	s_nop 1
	v_mov_b32_e32 v2, vcc_lo
	v_mov_b32_e32 v9, vcc_hi
	v_cmp_ne_u32_e32 vcc, 0, v221
	v_cndmask_b32_e64 v2, 0, v2, s[22:23]
	v_cndmask_b32_e64 v9, 0, v9, s[22:23]
	v_mov_b32_e32 v11, vcc_hi
	v_mov_b32_e32 v14, vcc_lo
	v_cndmask_b32_e64 v9, v9, v11, s[6:7]
	v_cndmask_b32_e64 v2, v2, v14, s[6:7]
	v_cmp_ne_u32_e32 vcc, 0, v222
	s_nop 1
	v_mov_b32_e32 v11, vcc_lo
	v_mov_b32_e32 v14, vcc_hi
	v_cmp_ne_u32_e32 vcc, 0, v223
	v_cndmask_b32_e64 v2, v2, v11, s[8:9]
	v_cndmask_b32_e64 v9, v9, v14, s[8:9]
	v_mov_b32_e32 v11, vcc_hi
	v_mov_b32_e32 v14, vcc_lo
	v_cmp_ne_u32_e32 vcc, 0, v224
	v_cndmask_b32_e64 v9, v9, v11, s[10:11]
	v_cndmask_b32_e64 v2, v2, v14, s[10:11]
	v_mov_b32_e32 v11, vcc_lo
	v_mov_b32_e32 v12, vcc_hi
	v_cmp_ne_u32_e32 vcc, 0, v225
	v_cndmask_b32_e64 v2, v2, v11, s[12:13]
	v_cndmask_b32_e64 v9, v9, v12, s[12:13]
	v_mov_b32_e32 v11, vcc_hi
	v_mov_b32_e32 v12, vcc_lo
	v_cndmask_b32_e64 v9, v9, v11, s[14:15]
	v_cndmask_b32_e64 v2, v2, v12, s[14:15]
	v_cmp_ne_u32_e32 vcc, 0, v226
	s_nop 1
	v_mov_b32_e32 v10, vcc_lo
	v_mov_b32_e32 v11, vcc_hi
	v_cmp_ne_u32_e32 vcc, 0, v227
	v_cndmask_b32_e64 v2, v2, v10, s[16:17]
	v_cndmask_b32_e64 v8, v9, v11, s[16:17]
	v_mov_b32_e32 v9, vcc_hi
	v_mov_b32_e32 v10, vcc_lo
	v_cndmask_b32_e64 v9, v8, v9, s[18:19]
	v_cndmask_b32_e64 v8, v2, v10, s[18:19]
	s_mov_b64 s[2:3], exec
	s_mov_b64 exec, s[0:1]
	global_store_dwordx2 v[4:5], v[8:9], off
	s_mov_b64 exec, s[2:3]
	v_cmp_ne_u64_e32 vcc, 0, v[8:9]
	s_and_b64 s[20:21], s[0:1], vcc
	s_cmp_lg_u64 s[20:21], 0
	s_cselect_b32 s20, 32768, 0
	s_or_b32 s76, s76, s20
	v_cmp_ne_u64_e32 vcc, -1, v[8:9]
	s_and_b64 s[20:21], s[0:1], vcc
	s_cmp_lg_u64 s[20:21], 0
	s_cselect_b32 s20, 32768, 0
	s_or_b32 s77, s77, s20
	v_lshl_add_u64 v[4:5], v[4:5], 0, 8
	v_mov_b32_e32 v2, s76
	v_mov_b32_e32 v8, s77
	s_mov_b64 s[2:3], exec
	s_mov_b64 exec, s[22:23]
	ds_write2_b32 v1, v2, v8 offset1:8
	s_mov_b64 exec, s[2:3]
	s_waitcnt lgkmcnt(0)
	s_barrier
	ds_read_b128 v[8:11], v3
	ds_read_b128 v[12:15], v3 offset:16
	ds_read_b128 v[16:19], v3 offset:32
	ds_read_b128 v[20:23], v3 offset:48
	s_waitcnt lgkmcnt(0)
	v_or_b32_e32 v8, v8, v9
	v_or3_b32 v8, v8, v10, v11
	v_or3_b32 v8, v8, v12, v13
	v_or3_b32 v8, v8, v14, v15
	v_or_b32_e32 v16, v16, v17
	v_or3_b32 v16, v16, v18, v19
	v_or3_b32 v16, v16, v20, v21
	v_or3_b32 v16, v16, v22, v23
	v_and_b32_e32 v2, 15, v0
	v_lshrrev_b32_e32 v8, v2, v8
	v_and_b32_e32 v8, 1, v8
	v_lshrrev_b32_e32 v16, v2, v16
	v_and_b32_e32 v16, 1, v16
	v_lshl_or_b32 v8, v16, 1, v8
	v_lshlrev_b32_e32 v2, 2, v2
	v_cmp_gt_u32_e32 vcc, 16, v0
	s_and_saveexec_b64 s[2:3], vcc
	global_store_dword v2, v8, s[26:27]
	s_mov_b64 exec, s[2:3]
